# MLA: 5-slot LDS ring (side-job tile at 0x1e000), DMA lead of four stages, stage-barrier wait leaves the latest stage's 3 pieces in flight
# baseline (speedup 1.0000x reference)
; #define LAS __attribute__((address_space(3)))
; #define WAITV(n) asm volatile("s_waitcnt vmcnt(%0)" ::"n"(n) : "memory")
; #define SBAR() do { asm volatile("s_waitcnt lgkmcnt(0)" ::: "memory"); __builtin_amdgcn_s_barrier(); asm volatile("" ::: "memory"); } while (0)
; DEV int otid() { int t = threadIdx.x; asm volatile("" : "+v"(t)); return t; }
; DEV unsigned char* ows_(unsigned char* w) { gptr_t g = (gptr_t)w; asm volatile("" : "+s"(g)); return (unsigned char*)g; }
; DEV unsigned lds_addr(LAS char* p) { return (unsigned)(uintptr_t)p; }
; #define MFMA8(a, b, c) __builtin_amdgcn_mfma_scale_f32_32x32x64_f8f6f4((a), (b), (c), 0, 0, 0, 0x7f7f7f7f, 0, 0x7c7c7c7c)
; template <int VAR> DEV void mla_unit(const Params& p, int layer, int b, int hd, int tokbase, int t0, int t1, LAS char* lds, SideJob& sj) {
;     unsigned char* ws = ows_(p.ws); const int tid = otid(), lane = tid & 63, wid = tid >> 6, r = lane & 31, h = lane >> 5;
;     constexpr int STG = MLA_IMG;
;     const float cinit = 15.0f - ((const float*)(ws + WS_SCAL))[layer * 8 + 1];
;     const int tok = tokbase + 32 * wid + r;
;     v8i qf[2];
; #pragma unroll
;     for (int sx = 0; sx < 2; ++sx) { const u32x4* q8 = (const u32x4*)(ws + WS_QC + (size_t)tok * 768 + hd * 128 + 64 * sx + 32 * h); const u32x4 a = q8[0], bq = q8[1];
;         qf[sx] = (v8i){(int)a[0], (int)a[1], (int)a[2], (int)a[3], (int)bq[0], (int)bq[1], (int)bq[2], (int)bq[3]}; }
;     const unsigned char* imgs = ws + WS_KVC + (size_t)((b * 6 + hd) * 130) * MLA_IMG;
;     const unsigned ldsw = (unsigned)__builtin_amdgcn_readfirstlane((int)(lds_addr(lds) + (unsigned)(wid * (STG / 8))));
;     ...
;     f32x16 cini, sA0, sA1, sB0, sB1, o0, o1, lacc;
; #pragma unroll
;     for (int i = 0; i < 16; ++i) { cini[i] = cinit; o0[i] = 0.f; o1[i] = 0.f; lacc[i] = 0.f; }
;     const unsigned koffl = (unsigned)(2 * h * 1024 + r * 16);
;     const unsigned voffl = (unsigned)MLA_VOFF + (unsigned)(2 * h * 1024 + r * 16);
;     const int ns = t1 - t0;
;     MLA_ISSUE(t0, 0);
;     WAITV(0); SBAR();
;     if (ns > 1) MLA_ISSUE(t0 + 1, 1);
;     { LAS char* kp = lds + koffl;
;       sA0 = MFMA8(mla_kf8(kp, 0, 0), qf[0], cini); sA1 = MFMA8(mla_kf8(kp, 1, 0), qf[0], cini);
.LBB0_758:
	s_mov_b64 s[8:9], 0
	s_and_b64 vcc, exec, s[6:7]
	s_cbranch_vccz .LBB0_765
	s_cmpk_gt_i32 s64, 0x2ff
	s_mov_b64 s[6:7], -1
	s_cbranch_scc0 .LBB0_808
	s_add_i32 s2, s64, 0xfffffd00
	s_mul_hi_u32 s3, s2, 0xaaaaaaab
	s_lshr_b32 s3, s3, 2
	s_mul_i32 s6, s3, 6
	s_sub_i32 s30, s2, s6
	s_lshl_b32 s3, s3, 8
	s_mov_b64 s[6:7], s[38:39]
	v_mov_b32_e32 v6, v246
	s_add_i32 s3, s3, 0x8000
	s_lshl_b64 s[8:9], s[48:49], 2
	v_and_b32_e32 v9, 31, v6
	v_ashrrev_i32_e32 v7, 6, v6
	v_or_b32_e32 v2, s3, v9
	s_add_u32 s8, s6, s8
	v_lshl_add_u32 v138, v7, 5, v2
	v_mov_b64_e32 v[2:3], s[6:7]
	s_movk_i32 s3, 0x300
	s_addc_u32 s9, s7, s9
	v_mad_i64_i32 v[2:3], s[20:21], v138, s3, v[2:3]
	s_lshl_b32 s30, s30, 7
	v_lshl_add_u64 v[2:3], v[2:3], 0, s[30:31]
	v_and_b32_e32 v178, 32, v6
	v_lshl_add_u64 v[2:3], v[2:3], 0, v[178:179]
	s_mov_b64 s[20:21], 0x33370100
	s_mov_b32 s3, 0x33370000
	v_lshl_add_u64 v[4:5], v[2:3], 0, s[20:21]
	v_add_co_u32_e32 v2, vcc, s3, v2
	s_mul_i32 s3, s2, 0x82
	s_nop 0
	v_addc_co_u32_e32 v3, vcc, 0, v3, vcc
	global_load_dwordx4 v[122:125], v[2:3], off offset:256
	global_load_dword v8, v247, s[8:9] offset:4
	global_load_dwordx4 v[126:129], v[4:5], off offset:16
	global_load_dwordx4 v[118:121], v[4:5], off offset:80
	global_load_dwordx4 v[114:117], v[4:5], off offset:64
	s_mul_i32 s2, s2, 0x30c000
	s_movk_i32 s8, 0xc00
	s_mul_hi_u32 s3, s3, 0x6000
	v_mul_lo_u32 v2, v7, s8
	v_bfe_u32 v140, v6, 5, 1
	s_add_u32 s8, s6, s2
	v_lshlrev_b32_e32 v3, 4, v9
	v_and_b32_e32 v4, 63, v6
	s_addc_u32 s9, s7, s3
	v_lshl_or_b32 v7, v140, 11, v3
	v_ashrrev_i32_e32 v3, 31, v2
	v_readfirstlane_b32 s20, v2
	v_lshlrev_b32_e32 v178, 4, v4
	v_lshl_add_u64 v[2:3], s[8:9], 0, v[2:3]
	v_lshl_add_u64 v[2:3], v[2:3], 0, v[178:179]
	s_mov_b64 s[8:9], 0x35b00100
	s_add_i32 s2, s20, 0
	v_lshl_add_u64 v[4:5], v[2:3], 0, s[8:9]
	s_mov_b32 s3, m0
	s_mov_b32 m0, s2
	s_nop 0
	global_load_lds_dwordx4 v[4:5], off
	s_mov_b32 m0, s3
	s_mov_b64 s[8:9], 0x35b00500
	v_lshl_add_u64 v[4:5], v[2:3], 0, s[8:9]
	s_add_i32 s3, s2, 0x400
	s_mov_b32 s8, m0
	s_mov_b32 m0, s3
	s_nop 0
	global_load_lds_dwordx4 v[4:5], off
	s_mov_b32 m0, s8
	s_mov_b64 s[8:9], 0x35b00900
	v_lshl_add_u64 v[4:5], v[2:3], 0, s[8:9]
	s_add_i32 s3, s2, 0x800
	s_mov_b32 s8, m0
	s_mov_b32 m0, s3
	s_nop 0
	global_load_lds_dwordx4 v[4:5], off
	s_mov_b32 m0, s8
	s_waitcnt vmcnt(0)
	s_waitcnt lgkmcnt(0)
	s_barrier
	s_mov_b64 s[8:9], 0x35b06100
	v_lshl_add_u64 v[4:5], v[2:3], 0, s[8:9]
	s_add_i32 s3, s2, 0x6000
	s_mov_b32 s8, m0
	s_mov_b32 m0, s3
	s_nop 0
	global_load_lds_dwordx4 v[4:5], off
	s_mov_b32 m0, s8
	s_mov_b64 s[8:9], 0x35b06500
	v_lshl_add_u64 v[4:5], v[2:3], 0, s[8:9]
	s_add_i32 s3, s2, 0x6400
	s_mov_b32 s8, m0
	s_mov_b32 m0, s3
	s_nop 0
	global_load_lds_dwordx4 v[4:5], off
	s_mov_b32 m0, s8
	s_mov_b64 s[8:9], 0x35b06900
	v_lshl_add_u64 v[2:3], v[2:3], 0, s[8:9]
	s_addk_i32 s2, 0x6800
	s_mov_b32 s3, m0
	s_mov_b32 m0, s2
	s_nop 0
	global_load_lds_dwordx4 v[2:3], off
	s_mov_b32 m0, s3
	v_add_u32_e32 v141, 0, v7
	ds_read_b128 v[18:21], v141
	ds_read_b128 v[34:37], v141 offset:512
	ds_read_b128 v[22:25], v141 offset:1024
	ds_read_b128 v[38:41], v141 offset:1536
	ds_read_b128 v[58:61], v141 offset:4096
	ds_read_b128 v[50:53], v141 offset:4608
	ds_read_b128 v[62:65], v141 offset:5120
	ds_read_b128 v[54:57], v141 offset:5632
	v_ashrrev_i32_e32 v76, 4, v6
	s_movk_i32 s2, 0x104
	v_mul_lo_u32 v3, v76, s2
	s_add_i32 s2, 0, 0x1e000
	s_and_b32 s37, s29, 3
	v_lshlrev_b32_e32 v2, 2, v6
	s_cmp_gt_i32 s33, 63
	v_and_b32_e32 v2, 60, v2
	s_cselect_b64 s[8:9], -1, 0
	s_cmp_eq_u32 s37, 3
	v_lshlrev_b32_e32 v74, 2, v2
	v_cmp_lt_u32_e64 s[40:41], 31, v2
	v_lshlrev_b32_e32 v2, 3, v6
	s_cselect_b64 s[20:21], -1, 0
	v_ashrrev_i32_e32 v78, 3, v6
	v_and_b32_e32 v178, 56, v2
	s_or_b64 s[8:9], s[8:9], s[20:21]
	s_waitcnt vmcnt(0)
	v_mov_b64_e32 v[192:193], v[188:189]
	v_mov_b64_e32 v[196:197], v[184:185]
	v_add3_u32 v77, s2, v3, v74
	v_lshl_add_u32 v79, v78, 2, s2
	v_mul_u32_u24_e32 v80, 0x104, v178
	s_and_b64 vcc, exec, s[8:9]
	v_mov_b64_e32 v[190:191], v[186:187]
	v_mov_b64_e32 v[194:195], v[182:183]
	s_mov_b32 s62, s36
	s_mov_b32 s63, s33
	s_cbranch_vccnz .LBB0_783
	s_add_i32 s20, s33, s12
	s_cmpk_lt_i32 s36, 0x100
	s_cselect_b64 s[50:51], -1, 0
	s_lshl_b32 s55, s36, 6
	s_cmpk_gt_i32 s36, 0xff
	s_mov_b64 s[58:59], -1
	s_cbranch_scc1 .LBB0_763
	s_ashr_i32 s21, s20, 31
	s_lshl_b64 s[52:53], s[20:21], 21
	s_add_u32 s8, s44, s52
	s_addc_u32 s9, s45, s53
	s_add_u32 s52, s46, s52
	s_addc_u32 s53, s47, s53
	s_lshl_b64 s[56:57], s[20:21], 20
	s_add_u32 s56, s13, s56
	s_addc_u32 s57, s16, s57
	s_and_b32 s54, s55, 0x3c0
	s_ashr_i32 s65, s36, 4
	s_mov_b64 s[58:59], 0

; #define WAITV(n) asm volatile("s_waitcnt vmcnt(%0)" ::"n"(n) : "memory")
; #define SBAR() do { asm volatile("s_waitcnt lgkmcnt(0)" ::: "memory"); __builtin_amdgcn_s_barrier(); asm volatile("" ::: "memory"); } while (0)
; DEV int otid() { int t = threadIdx.x; asm volatile("" : "+v"(t)); return t; }
; DEV unsigned char* ows_(unsigned char* w) { gptr_t g = (gptr_t)w; asm volatile("" : "+s"(g)); return (unsigned char*)g; }
; DEV unsigned lds_addr(LAS char* p) { return (unsigned)(uintptr_t)p; }
; #define MLA_ISSUE(t_, st_) do { const unsigned char* s_ = imgs + (size_t)(t_) * MLA_IMG + wid * (STG / 8) + lane * 16; const unsigned d_ = ldsw + (unsigned)((st_) * STG); \
;     _Pragma("unroll") for (int i_ = 0; i_ < STG / 8192; ++i_) glds16a(s_ + i_ * 1024, d_ + i_ * 1024); } while (0)
; template <int VAR> DEV void mla_unit(const Params& p, int layer, int b, int hd, int tokbase, int t0, int t1, LAS char* lds, SideJob& sj) {
;     unsigned char* ws = ows_(p.ws); const int tid = otid(), lane = tid & 63, wid = tid >> 6, r = lane & 31, h = lane >> 5;
;     constexpr int STG = MLA_IMG;
;     const float cinit = 15.0f - ((const float*)(ws + WS_SCAL))[layer * 8 + 1];
;     const int tok = tokbase + 32 * wid + r;
;     v8i qf[2];
; #pragma unroll
;     for (int sx = 0; sx < 2; ++sx) { const u32x4* q8 = (const u32x4*)(ws + WS_QC + (size_t)tok * 768 + hd * 128 + 64 * sx + 32 * h); const u32x4 a = q8[0], bq = q8[1];
;         qf[sx] = (v8i){(int)a[0], (int)a[1], (int)a[2], (int)a[3], (int)bq[0], (int)bq[1], (int)bq[2], (int)bq[3]}; }
;     const unsigned char* imgs = ws + WS_KVC + (size_t)((b * 6 + hd) * 130) * MLA_IMG;
;     const unsigned ldsw = (unsigned)__builtin_amdgcn_readfirstlane((int)(lds_addr(lds) + (unsigned)(wid * (STG / 8))));
;     ...
;     f32x16 cini, sA0, sA1, sB0, sB1, o0, o1, lacc;
; #pragma unroll
;     for (int i = 0; i < 16; ++i) { cini[i] = cinit; o0[i] = 0.f; o1[i] = 0.f; lacc[i] = 0.f; }
;     const unsigned koffl = (unsigned)(2 * h * 1024 + r * 16);
;     const unsigned voffl = (unsigned)MLA_VOFF + (unsigned)(2 * h * 1024 + r * 16);
;     const int ns = t1 - t0;
;     MLA_ISSUE(t0, 0);
;     WAITV(0); SBAR();
.LBB0_808:
	s_and_b64 vcc, exec, s[6:7]
	s_cbranch_vccz .LBB0_749
	s_ashr_i32 s2, s64, 6
	s_mul_hi_i32 s3, s2, 0x2aaaaaab
	s_lshr_b32 s6, s3, 31
	s_add_i32 s3, s3, s6
	s_mul_i32 s6, s3, 6
	s_sub_i32 s37, s2, s6
	s_lshl_b32 s6, s64, 8
	s_lshl_b32 s3, s3, 14
	s_and_b32 s6, s6, 0x3f00
	s_or_b32 s3, s3, s6
	s_mov_b64 s[6:7], s[38:39]
	v_mov_b32_e32 v52, v246
	s_lshl_b64 s[8:9], s[48:49], 2
	v_and_b32_e32 v7, 31, v52
	v_ashrrev_i32_e32 v6, 6, v52
	s_add_u32 s8, s6, s8
	v_or_b32_e32 v2, s3, v7
	s_addc_u32 s9, s7, s9
	v_lshl_add_u32 v180, v6, 5, v2
	v_mov_b64_e32 v[2:3], s[6:7]
	s_movk_i32 s3, 0x300
	global_load_dword v8, v247, s[8:9] offset:4
	v_mad_i64_i32 v[2:3], s[8:9], v180, s3, v[2:3]
	s_lshl_b32 s8, s37, 7
	s_ashr_i32 s9, s8, 31
	v_lshl_add_u64 v[2:3], v[2:3], 0, s[8:9]
	v_and_b32_e32 v178, 32, v52
	v_lshl_add_u64 v[2:3], v[2:3], 0, v[178:179]
	s_mov_b64 s[8:9], 0x33370100
	s_mov_b32 s3, 0x33370000
	v_lshl_add_u64 v[4:5], v[2:3], 0, s[8:9]
	v_add_co_u32_e32 v2, vcc, s3, v2
	s_mul_i32 s3, s2, 0x82
	s_nop 0
	v_addc_co_u32_e32 v3, vcc, 0, v3, vcc
	global_load_dwordx4 v[138:141], v[2:3], off offset:256
	global_load_dwordx4 v[142:145], v[4:5], off offset:16
	global_load_dwordx4 v[134:137], v[4:5], off offset:80
	global_load_dwordx4 v[130:133], v[4:5], off offset:64
	s_mul_i32 s8, s2, 0x30c000
	s_movk_i32 s2, 0xc00
	s_mul_hi_i32 s9, s3, 0x6000
	v_mul_lo_u32 v50, v6, s2
	s_add_u32 s20, s6, s8
	v_and_b32_e32 v3, 63, v52
	v_bfe_u32 v198, v52, 5, 1
	s_addc_u32 s21, s7, s9
	v_lshlrev_b32_e32 v4, 4, v7
	v_ashrrev_i32_e32 v51, 31, v50
	v_lshl_or_b32 v199, v198, 11, v4
	v_lshl_add_u64 v[4:5], s[20:21], 0, v[50:51]
	v_lshlrev_b32_e32 v178, 4, v3
	v_readfirstlane_b32 s60, v50
	v_lshl_add_u64 v[18:19], v[4:5], 0, v[178:179]
	s_mov_b64 s[20:21], 0x35800100
	s_add_i32 s60, s60, 0
	v_lshl_add_u64 v[4:5], v[18:19], 0, s[20:21]
	s_mov_b32 s2, m0
	s_mov_b32 m0, s60
	s_nop 0
	global_load_lds_dwordx4 v[4:5], off
	s_mov_b32 m0, s2
	s_mov_b64 s[20:21], 0x35800500
	v_lshl_add_u64 v[4:5], v[18:19], 0, s[20:21]
	s_add_i32 s2, s60, 0x400
	s_mov_b32 s3, m0
	s_mov_b32 m0, s2
	s_nop 0
	global_load_lds_dwordx4 v[4:5], off
	s_mov_b32 m0, s3
	s_mov_b64 s[20:21], 0x35800900
	v_lshl_add_u64 v[4:5], v[18:19], 0, s[20:21]
	s_add_i32 s2, s60, 0x800
	s_mov_b32 s3, m0
	s_mov_b32 m0, s2
	s_nop 0
	global_load_lds_dwordx4 v[4:5], off
	s_mov_b32 m0, s3
	s_waitcnt vmcnt(0)
	s_waitcnt lgkmcnt(0)
	s_barrier
; #define LAS __attribute__((address_space(3)))
; #define WAITV(n) asm volatile("s_waitcnt vmcnt(%0)" ::"n"(n) : "memory")
; #define SBAR() do { asm volatile("s_waitcnt lgkmcnt(0)" ::: "memory"); __builtin_amdgcn_s_barrier(); asm volatile("" ::: "memory"); } while (0)
; DEV float ex2(float x) { return __builtin_amdgcn_exp2f(x); }
; DEV unsigned lds_addr(LAS char* p) { return (unsigned)(uintptr_t)p; }
; #define MFMA8(a, b, c) __builtin_amdgcn_mfma_scale_f32_32x32x64_f8f6f4((a), (b), (c), 0, 0, 0, 0x7f7f7f7f, 0, 0x7c7c7c7c)
; #define MLA_ISSUE(t_, st_) do { const unsigned char* s_ = imgs + (size_t)(t_) * MLA_IMG + wid * (STG / 8) + lane * 16; const unsigned d_ = ldsw + (unsigned)((st_) * STG); \
;     _Pragma("unroll") for (int i_ = 0; i_ < STG / 8192; ++i_) glds16a(s_ + i_ * 1024, d_ + i_ * 1024); } while (0)
; template <int VAR> DEV void mla_unit(const Params& p, int layer, int b, int hd, int tokbase, int t0, int t1, LAS char* lds, SideJob& sj) {
;     ...
;     const unsigned ldsw = (unsigned)__builtin_amdgcn_readfirstlane((int)(lds_addr(lds) + (unsigned)(wid * (STG / 8))));
;     ...
;     f32x16 cini, sA0, sA1, sB0, sB1, o0, o1, lacc;
; #pragma unroll
;     for (int i = 0; i < 16; ++i) { cini[i] = cinit; o0[i] = 0.f; o1[i] = 0.f; lacc[i] = 0.f; }
;     const unsigned koffl = (unsigned)(2 * h * 1024 + r * 16);
;     const unsigned voffl = (unsigned)MLA_VOFF + (unsigned)(2 * h * 1024 + r * 16);
;     const int ns = t1 - t0;
;     MLA_ISSUE(t0, 0);
;     WAITV(0); SBAR();
;     if (ns > 1) MLA_ISSUE(t0 + 1, 1);
;     { LAS char* kp = lds + koffl;
;       sA0 = MFMA8(mla_kf8(kp, 0, 0), qf[0], cini); sA1 = MFMA8(mla_kf8(kp, 1, 0), qf[0], cini);
;       sA0 = MFMA8(mla_kf8(kp, 0, 1), qf[1], sA0); sA1 = MFMA8(mla_kf8(kp, 1, 1), qf[1], sA1);
; #pragma unroll
;       for (int i = 0; i < 16; ++i) { sA0[i] = ex2(sA0[i]); sA1[i] = ex2(sA1[i]); } }
;     int slot = 0;
	s_mov_b64 s[20:21], 0x35806100
	v_lshl_add_u64 v[20:21], v[18:19], 0, s[20:21]
	s_add_i32 s2, s60, 0x6000
	s_mov_b32 s3, m0
	s_mov_b32 m0, s2
	s_nop 0
	global_load_lds_dwordx4 v[20:21], off
	s_mov_b32 m0, s3
	s_mov_b64 s[20:21], 0x35806500
	v_lshl_add_u64 v[20:21], v[18:19], 0, s[20:21]
	s_add_i32 s2, s60, 0x6400
	s_mov_b32 s3, m0
	s_mov_b32 m0, s2
	s_nop 0
	global_load_lds_dwordx4 v[20:21], off
	s_mov_b32 m0, s3
	s_mov_b64 s[20:21], 0x35806900
	v_lshl_add_u64 v[18:19], v[18:19], 0, s[20:21]
	s_add_i32 s2, s60, 0x6800
	s_mov_b32 s3, m0
	s_mov_b32 m0, s2
	s_nop 0
	global_load_lds_dwordx4 v[18:19], off
	s_mov_b32 m0, s3
	v_add_u32_e32 v200, 0, v199
	ds_read_b128 v[18:21], v200
	ds_read_b128 v[22:25], v200 offset:1024
	s_waitcnt vmcnt(3)
	v_ashrrev_i32_e32 v191, 4, v52
	s_movk_i32 s2, 0x104
	v_ashrrev_i32_e32 v195, 3, v52
	v_ashrrev_i32_e32 v181, 31, v180
	s_mov_b32 s62, 0
	v_mov_b32_e32 v193, v179
	v_mov_b32_e32 v146, 0
	v_mov_b32_e32 v147, 0
	v_mov_b32_e32 v148, 0
	v_mov_b32_e32 v149, 0
	v_mov_b32_e32 v150, 0
	v_mov_b32_e32 v151, 0
	v_mov_b32_e32 v152, 0
	v_mov_b32_e32 v153, 0
	s_mov_b32 s61, 0
	v_sub_f32_e32 v2, 0x41700000, v8
	v_mov_b32_e32 v3, v2
	v_mov_b32_e32 v4, v2
	v_mov_b32_e32 v5, v2
	v_mov_b32_e32 v6, v2
	v_mov_b32_e32 v7, v2
	v_mov_b32_e32 v8, v2
	v_mov_b32_e32 v9, v2
	v_mov_b32_e32 v10, v2
	v_mov_b32_e32 v11, v2
	v_mov_b32_e32 v12, v2
	v_mov_b32_e32 v13, v2
	v_mov_b32_e32 v14, v2
	v_mov_b32_e32 v15, v2
	v_mov_b32_e32 v16, v2
	v_mov_b32_e32 v17, v2
	s_waitcnt lgkmcnt(0)
	s_nop 0
	v_mfma_scale_f32_32x32x64_f8f6f4 v[18:33], v[18:25], v[138:145], v[2:17], v209, v208 op_sel_hi:[0,0,0]
	ds_read_b128 v[34:37], v200 offset:512
	ds_read_b128 v[38:41], v200 offset:1536
	s_waitcnt lgkmcnt(0)
	v_mfma_scale_f32_32x32x64_f8f6f4 v[34:49], v[34:41], v[138:145], v[2:17], v209, v208 op_sel_hi:[0,0,0]
	ds_read_b128 v[54:57], v200 offset:4096
	ds_read_b128 v[58:61], v200 offset:5120
	s_waitcnt lgkmcnt(0)
	v_mfma_scale_f32_32x32x64_f8f6f4 v[18:33], v[54:61], v[130:137], v[18:33], v209, v208 op_sel_hi:[0,0,0]
	ds_read_b128 v[54:57], v200 offset:4608
	ds_read_b128 v[58:61], v200 offset:5632
	s_waitcnt lgkmcnt(0)
	v_mfma_scale_f32_32x32x64_f8f6f4 v[34:49], v[54:61], v[130:137], v[34:49], v209, v208 op_sel_hi:[0,0,0]
	s_nop 15
	v_exp_f32_e32 v82, v18
	v_lshlrev_b32_e32 v18, 2, v52
	v_and_b32_e32 v190, 60, v18
	v_exp_f32_e32 v83, v19
	v_mul_lo_u32 v18, v191, s2
	s_add_i32 s2, 0, 0x1e000
	v_lshlrev_b32_e32 v19, 2, v190
	v_add3_u32 v194, s2, v18, v19
	v_lshlrev_b32_e32 v18, 3, v52
	v_exp_f32_e32 v84, v20
	v_exp_f32_e32 v85, v21
	v_exp_f32_e32 v86, v22
	v_exp_f32_e32 v87, v23
	v_exp_f32_e32 v88, v24
	v_exp_f32_e32 v89, v25
	v_exp_f32_e32 v66, v34
	v_exp_f32_e32 v67, v35
	v_exp_f32_e32 v68, v36
	v_mov_b32_e32 v69, v37
	v_mov_b32_e32 v70, v38
	v_mov_b32_e32 v71, v39
	v_mov_b32_e32 v72, v40
	v_mov_b32_e32 v73, v41
	v_mov_b32_e32 v74, v42
	v_mov_b32_e32 v75, v43
	v_mov_b32_e32 v76, v44
	v_mov_b32_e32 v77, v45
	v_mov_b32_e32 v78, v46
	v_mov_b32_e32 v79, v47
	v_mov_b32_e32 v80, v48
	v_mov_b32_e32 v81, v49
	v_exp_f32_e32 v90, v26
	v_exp_f32_e32 v91, v27
	v_exp_f32_e32 v92, v28
	v_exp_f32_e32 v93, v29
	v_exp_f32_e32 v94, v30
	v_exp_f32_e32 v95, v31
	v_exp_f32_e32 v96, v32
	v_exp_f32_e32 v97, v33
	v_and_b32_e32 v192, 56, v18
	v_or_b32_e32 v18, s8, v178
	v_mov_b32_e32 v19, s9
	v_lshl_add_u64 v[18:19], v[18:19], 0, v[50:51]
	v_lshl_add_u64 v[18:19], s[6:7], 0, v[18:19]
	s_mov_b64 s[8:9], 0x3580c100
	v_mov_b32_e32 v34, 0
	v_cmp_lt_u32_e64 s[40:41], 31, v190
	v_lshl_add_u32 v196, v195, 2, s2
	v_mul_u32_u24_e32 v197, 0x104, v192
	v_lshl_add_u64 v[162:163], v[18:19], 0, s[8:9]
	s_add_i32 s2, s60, 0xc000
	s_mov_b32 s3, m0
	s_mov_b32 m0, s2
	s_nop 0
	global_load_lds_dwordx4 v[162:163], off
	global_load_lds_dwordx4 v[162:163], off offset:1024
	global_load_lds_dwordx4 v[162:163], off offset:2048
	s_mov_b32 m0, s3
	s_mov_b64 s[8:9], 0x6000
	v_lshl_add_u64 v[162:163], v[162:163], 0, s[8:9]
	s_add_i32 s2, s60, 0x12000
	s_mov_b32 s3, m0
	s_mov_b32 m0, s2
	s_nop 0
	global_load_lds_dwordx4 v[162:163], off
	global_load_lds_dwordx4 v[162:163], off offset:1024
	global_load_lds_dwordx4 v[162:163], off offset:2048
	s_mov_b32 m0, s3
	v_lshl_add_u64 v[162:163], v[162:163], 0, s[8:9]
	v_mov_b32_e32 v35, v34
	v_mov_b32_e32 v36, v34
	v_mov_b32_e32 v37, v34
	v_mov_b32_e32 v38, v34
	v_mov_b32_e32 v39, v34
	v_mov_b32_e32 v40, v34
	v_mov_b32_e32 v41, v34
	v_mov_b32_e32 v42, v34
	v_mov_b32_e32 v43, v34
	v_mov_b32_e32 v44, v34
	v_mov_b32_e32 v45, v34
	v_mov_b32_e32 v46, v34
	v_mov_b32_e32 v47, v34
	v_mov_b32_e32 v48, v34
	v_mov_b32_e32 v49, v34
	v_mov_b32_e32 v18, v34
	v_mov_b32_e32 v19, v34
	v_mov_b32_e32 v20, v34
	v_mov_b32_e32 v21, v34
	v_mov_b32_e32 v22, v34
	v_mov_b32_e32 v23, v34
	v_mov_b32_e32 v24, v34
	v_mov_b32_e32 v25, v34
	v_mov_b32_e32 v26, v34
	v_mov_b32_e32 v27, v34
	v_mov_b32_e32 v28, v34
	v_mov_b32_e32 v29, v34
	v_mov_b32_e32 v30, v34
	v_mov_b32_e32 v31, v34
	v_mov_b32_e32 v32, v34
	v_mov_b32_e32 v33, v34
	v_mov_b32_e32 v50, v34
	v_mov_b32_e32 v51, v34
	v_mov_b32_e32 v52, v34
	v_mov_b32_e32 v53, v34
	v_mov_b32_e32 v54, v34
	v_mov_b32_e32 v55, v34
	v_mov_b32_e32 v56, v34
	v_mov_b32_e32 v57, v34
	v_mov_b32_e32 v58, v34
	v_mov_b32_e32 v59, v34
	v_mov_b32_e32 v60, v34
	v_mov_b32_e32 v61, v34
	v_mov_b32_e32 v62, v34
	v_mov_b32_e32 v63, v34
	v_mov_b32_e32 v64, v34
	v_mov_b32_e32 v65, v34
	s_waitcnt vmcnt(6)
	s_waitcnt lgkmcnt(0)
	s_barrier
	v_mov_b64_e32 v[210:211], s[76:77]
	v_mov_b64_e32 v[212:213], s[78:79]
	v_mov_b64_e32 v[214:215], s[80:81]
	v_mov_b64_e32 v[216:217], s[82:83]
	s_cmp_ge_u32 s60, 0x3000
	s_cbranch_scc0 .Lmla_prio_skip
	s_setprio 1

; #define LAS __attribute__((address_space(3)))
; #define WAITV(n) asm volatile("s_waitcnt vmcnt(%0)" ::"n"(n) : "memory")
; template <int VAR> DEV void mla_step(f32x16& C0, f32x16& C1, f32x16& P0, f32x16& P1, f32x16& o0, f32x16& o1, f32x16& lacc,
;                   const v8i (&qf)[2], const f32x16& cini, LAS char* kp, LAS char* vp, v8i& pw) {
;     v8i kf[2], vf[2];
;     const v8i ones8 = {0x38383838, 0x38383838, 0x38383838, 0x38383838, 0x38383838, 0x38383838, 0x38383838, 0x38383838};
;     kf[0] = mla_kf8(kp, 0, 0); kf[1] = mla_kf8(kp, 1, 0);
;     MLA_SB();
; #pragma unroll
;     for (int g = 0; g < 4; ++g) {
;         const int kb = g & 1, sx = g >> 1;
;         if (kb) C1 = MFMA8(kf[1], qf[sx], sx == 0 ? cini : C1); else C0 = MFMA8(kf[0], qf[sx], sx == 0 ? cini : C0);
;         if (g < 2) kf[kb] = mla_kf8(kp, kb, 1);
;         if (g >= 2) vf[g - 2] = mla_vf8(vp, g - 2);
; #pragma unroll
;         for (int j = 0; j < 2; ++j) { const int w = 2 * g + j, e = 4 * w;
;             if (VAR == 3) pw[w] = __builtin_bit_cast(int, (e < 16) ? P0[e] : P1[e - 16]);
;             else pw[w] = (int)((e < 16) ? pk_bf8x4(P0[e], P0[e + 1], P0[e + 2], P0[e + 3], pw[w]) : pk_bf8x4(P1[e - 16], P1[e - 15], P1[e - 14], P1[e - 13], pw[w])); }
;         if (g == 3) MLA_PIN(pw);
;         MLA_SB();
;     }
; #pragma unroll
;     for (int g = 0; g < 3; ++g) {
;         if (g == 0) o0 = MFMA8PV(vf[0], pw, o0); else if (g == 1) o1 = MFMA8PV(vf[1], pw, o1); else lacc = MFMA8PV(ones8, pw, lacc);
;         const int e0 = (g * 32) / 3, e1 = ((g + 1) * 32) / 3;
; #pragma unroll
;         for (int e = e0; e < e1; ++e) { if (VAR == 2 || VAR == 3) continue; if (e < 16) C0[e] = ex2(C0[e]); else C1[e - 16] = ex2(C1[e - 16]); }
;         if (g < 2) MLA_PIN(C0);
;         if (g > 0) MLA_PIN(C1);
;         MLA_SB();
;     }
; }
; template <int VAR> DEV void mla_unit(const Params& p, int layer, int b, int hd, int tokbase, int t0, int t1, LAS char* lds, SideJob& sj) {
;     ...
;     for (int s = 0; s < ns; ++s) {
;         sj_tick(p, layer, sj, lds, tid);
;         { LAS char* base = lds + slot * STG; mla_step<VAR>(sB0, sB1, sA0, sA1, o0, o1, lacc, qf, cini, base + MLA_KSUB + koffl, base + voffl, pw); }
;         if (s + 1 < ns) {
;             const int nslot = (slot == 2) ? 0 : slot + 1;
;             WAITV(0); SBAR();
;             if (s + 2 < ns) MLA_ISSUE(t0 + s + 2, (nslot == 2) ? 0 : nslot + 1);
.LBB0_812:
	s_mul_i32 s2, s62, 0x6000
	v_add_u32_e32 v172, s2, v200
	s_add_i32 s3, s62, 1
	s_cmp_eq_u32 s3, 5
	s_cselect_b32 s3, 0, s3
	s_mul_i32 s3, s3, 0x6000
	ds_read_b128 v[98:101], v172 offset:8192
	ds_read_b128 v[106:109], v172 offset:8704
	ds_read_b128 v[102:105], v172 offset:9216
	ds_read_b128 v[110:113], v172 offset:9728
	v_cvt_pk_bf8_f32 v146, v82, v83
	v_cvt_pk_bf8_f32 v147, v86, v87
	v_exp_f32_e32 v69, v69
	v_exp_f32_e32 v70, v70
	v_exp_f32_e32 v71, v71
	s_waitcnt lgkmcnt(1)
	v_mfma_scale_f32_32x32x64_f8f6f4 v[114:129], v[98:105], v[138:145], v[2:17], v209, v208 op_sel_hi:[0,0,0]
	ds_read_b128 v[154:157], v172 offset:12288
	ds_read_b128 v[158:161], v172 offset:13312
	v_cvt_pk_bf8_f32 v146, v84, v85 op_sel:[0,0,1]
	v_cvt_pk_bf8_f32 v147, v88, v89 op_sel:[0,0,1]
	v_cvt_pk_bf8_f32 v148, v90, v91
	v_cvt_pk_bf8_f32 v149, v94, v95
	ds_read_b128 v[82:85], v172 offset:12800
	ds_read_b128 v[86:89], v172 offset:13824
	v_exp_f32_e32 v72, v72
	v_exp_f32_e32 v73, v73
	s_waitcnt lgkmcnt(4)
	v_mfma_scale_f32_32x32x64_f8f6f4 v[98:113], v[106:113], v[138:145], v[2:17], v209, v208 op_sel_hi:[0,0,0]
	v_cvt_pk_bf8_f32 v148, v92, v93 op_sel:[0,0,1]
	v_cvt_pk_bf8_f32 v149, v96, v97 op_sel:[0,0,1]
	ds_read_b128 v[90:93], v172 offset:16384
	ds_read_b128 v[94:97], v172 offset:17408
	v_exp_f32_e32 v74, v74
	v_exp_f32_e32 v75, v75
	v_exp_f32_e32 v76, v76
	s_waitcnt lgkmcnt(4)
	v_mfma_scale_f32_32x32x64_f8f6f4 v[114:129], v[154:161], v[130:137], v[114:129], v209, v208 op_sel_hi:[0,0,0]
	v_exp_f32_e32 v77, v77
	v_exp_f32_e32 v78, v78
	v_exp_f32_e32 v79, v79
	v_exp_f32_e32 v80, v80
	v_exp_f32_e32 v81, v81
	s_waitcnt lgkmcnt(2)
	v_mfma_scale_f32_32x32x64_f8f6f4 v[98:113], v[82:89], v[130:137], v[98:113], v209, v208 op_sel_hi:[0,0,0]
	v_cvt_pk_bf8_f32 v150, v66, v67
	v_cvt_pk_bf8_f32 v151, v70, v71
	v_cvt_pk_bf8_f32 v150, v68, v69 op_sel:[0,0,1]
	v_cvt_pk_bf8_f32 v151, v72, v73 op_sel:[0,0,1]
	v_cvt_pk_bf8_f32 v152, v74, v75
	v_cvt_pk_bf8_f32 v153, v78, v79
	v_cvt_pk_bf8_f32 v152, v76, v77 op_sel:[0,0,1]
	v_cvt_pk_bf8_f32 v153, v80, v81 op_sel:[0,0,1]
	ds_read_b128 v[66:69], v172 offset:16896
	ds_read_b128 v[70:73], v172 offset:17920
	s_waitcnt lgkmcnt(2)
	v_mfma_scale_f32_32x32x64_f8f6f4 v[50:65], v[90:97], v[146:153], v[50:65], v209, v209 op_sel_hi:[0,0,0] blgp:1
	s_nop 0
	v_exp_f32_e32 v114, v114
	v_exp_f32_e32 v115, v115
	v_exp_f32_e32 v116, v116
	v_exp_f32_e32 v117, v117
	v_exp_f32_e32 v118, v118
	v_exp_f32_e32 v119, v119
	v_add_u32_e32 v173, s3, v200
	ds_read_b128 v[74:77], v173 offset:512
	ds_read_b128 v[78:81], v173 offset:1536
	s_waitcnt lgkmcnt(2)
	v_mfma_scale_f32_32x32x64_f8f6f4 v[18:33], v[66:73], v[146:153], v[18:33], v209, v209 op_sel_hi:[0,0,0] blgp:1
	v_exp_f32_e32 v120, v120
	v_exp_f32_e32 v121, v121
	v_exp_f32_e32 v122, v122
	v_exp_f32_e32 v123, v123
	v_exp_f32_e32 v124, v124
	v_exp_f32_e32 v125, v125
	ds_read_b128 v[66:69], v173
	ds_read_b128 v[70:73], v173 offset:1024
	v_mfma_scale_f32_32x32x64_f8f6f4 v[34:49], v[210:217], v[146:153], v[34:49], v209, v209 op_sel_hi:[0,0,0] blgp:1
	v_exp_f32_e32 v126, v126
	v_exp_f32_e32 v127, v127
	v_exp_f32_e32 v128, v128
	v_exp_f32_e32 v129, v129
	v_exp_f32_e32 v98, v98
	v_exp_f32_e32 v99, v99
	v_exp_f32_e32 v100, v100
	s_add_i32 s61, s61, 1
	s_add_i32 s62, s62, 1
	s_cmp_eq_u32 s62, 5
	s_cselect_b32 s62, 0, s62
	s_mul_i32 s64, s62, 0x6000
	s_add_i32 s2, s62, 3
	s_add_i32 s3, s62, -2
	s_cmp_ge_u32 s2, 5
	s_cselect_b32 s2, s3, s2
	s_mul_i32 s2, s2, 0x6000
	s_cmp_eq_u32 s62, 4
	s_cselect_b64 s[8:9], -1, 0
	s_cmp_eq_u32 s100, 0
	s_cbranch_scc1 .Lmla_w0
	s_cmp_eq_u32 s100, 1
	s_cbranch_scc1 .Lmla_w1
	s_waitcnt vmcnt(5)
	s_branch .Lmla_wd
.Lmla_w1:
	s_waitcnt vmcnt(4)
	s_branch .Lmla_wd
.Lmla_w0:
	s_waitcnt vmcnt(3)
